# nt hint also on the P10 combine loads (expert output rows and x2 rows, each read once)
# speedup vs baseline: 1.0194x; 1.0027x over previous
; #define GAS __attribute__((address_space(1)))
; __device__ __forceinline__ void p10_final(Frame& F, const Args& A) {
;     ...
;     for (int t = gw; t < T; t += NGW) {
;         float v[16];
;         const int4 pi = *(const int4*)(pinf + 4 * t); const f32x4 pw4 = *(const f32x4*)(pwt + 4 * t);
;         const int pinfo4[4] = {pi.x, pi.y, pi.z, pi.w};
; #pragma unroll
;         for (int j = 0; j < 4; ++j) { const u32x2 w = *(const GAS u32x2*)(x2b + (size_t)t * D + 256 * j + 4 * lane);
;             v[4 * j] = bflo(w.x); v[4 * j + 1] = bfhi(w.x); v[4 * j + 2] = bflo(w.y); v[4 * j + 3] = bfhi(w.y); }
; #pragma unroll
;         for (int k = 0; k < 4; ++k) { const int e = pinfo4[k] & 31, pos = pinfo4[k] >> 5; const size_t row = (size_t)tpre[e] * 256 + pos; const float wk = pw4[k];
; #pragma unroll
;             for (int j = 0; j < 4; ++j) { const unsigned w = *(const GAS unsigned*)(Y + row * D + 256 * j + 4 * lane);
;                 const f32x2 a0 = __builtin_amdgcn_cvt_pk_f32_fp8((int)w, false), a1 = __builtin_amdgcn_cvt_pk_f32_fp8((int)w, true);
;                 v[4 * j] += wk * a0[0]; v[4 * j + 1] += wk * a0[1]; v[4 * j + 2] += wk * a1[0]; v[4 * j + 3] += wk * a1[1]; } }
.LBB0_1146:
	s_ashr_i32 s7, s6, 31
	s_lshl_b64 s[18:19], s[6:7], 2
	s_add_u32 s20, s12, s18
	s_addc_u32 s21, s13, s19
	s_add_u32 s18, s14, s18
	global_load_dwordx2 v[22:23], v[20:21], off offset:1024 nt
	global_load_dwordx2 v[28:29], v[20:21], off offset:1536 nt
	global_load_dwordx2 v[26:27], v[20:21], off nt
	global_load_dwordx2 v[24:25], v[20:21], off offset:512 nt
	s_addc_u32 s19, s15, s19
	global_load_dwordx4 v[32:35], v19, s[20:21]
	global_load_dwordx4 v[36:39], v19, s[18:19]
	s_add_i32 s30, s6, s16
	v_lshl_add_u64 v[120:121], v[20:21], 0, s[10:11]
	s_ashr_i32 s31, s30, 31
	s_lshl_b64 s[36:37], s[30:31], 2
	s_add_u32 s38, s12, s36
	s_addc_u32 s39, s13, s37
	s_add_u32 s36, s14, s36
	global_load_dwordx2 v[122:123], v[120:121], off offset:1024 nt
	global_load_dwordx2 v[128:129], v[120:121], off offset:1536 nt
	global_load_dwordx2 v[126:127], v[120:121], off nt
	global_load_dwordx2 v[124:125], v[120:121], off offset:512 nt
	s_addc_u32 s37, s15, s37
	global_load_dwordx4 v[132:135], v19, s[38:39]
	global_load_dwordx4 v[136:139], v19, s[36:37]
	s_add_i32 s0, s0, s2
	s_add_i32 s0, s0, s2
	s_add_i32 s6, s30, s16
	v_lshl_add_u64 v[20:21], v[120:121], 0, s[10:11]
	v_lshl_add_u64 v[118:119], v[0:1], 0, s[8:9]
	s_waitcnt vmcnt(7)
	v_and_b32_e32 v41, 0xffff0000, v23
	v_lshlrev_b32_e32 v40, 16, v23
	v_and_b32_e32 v43, 0xffff0000, v28
	v_lshlrev_b32_e32 v42, 16, v28
	v_readfirstlane_b32 s20, v32
	v_readfirstlane_b32 s7, v35
	v_readfirstlane_b32 s17, v34
	v_readfirstlane_b32 s19, v33
	s_and_b32 s21, s20, 31
	s_and_b32 s23, s19, 31
	s_ashr_i32 s22, s17, 5
	s_and_b32 s17, s17, 31
	s_ashr_i32 s24, s7, 5
	s_and_b32 s7, s7, 31
	s_lshl_b32 s26, s21, 2
	s_lshl_b32 s27, s23, 2
	s_lshl_b32 s17, s17, 2
	s_lshl_b32 s7, s7, 2
	s_add_i32 s26, s1, s26
	s_add_i32 s27, s1, s27
	s_add_i32 s17, s1, s17
	s_add_i32 s7, s1, s7
	v_mov_b32_e32 v23, s26
	v_mov_b32_e32 v31, s27
	v_mov_b32_e32 v33, s17
	v_mov_b32_e32 v35, s7
	ds_read_b32 v32, v23
	ds_read_b32 v34, v31
	ds_read_b32 v50, v33
	ds_read_b32 v52, v35
	s_ashr_i32 s18, s20, 5
	s_waitcnt lgkmcnt(3)
	v_ashrrev_i32_e32 v33, 31, v32
	s_ashr_i32 s20, s19, 5
	s_ashr_i32 s19, s18, 31
	s_waitcnt lgkmcnt(2)
	v_ashrrev_i32_e32 v35, 31, v34
	s_waitcnt lgkmcnt(1)
	v_ashrrev_i32_e32 v51, 31, v50
	s_waitcnt lgkmcnt(0)
	v_ashrrev_i32_e32 v53, 31, v52
	v_lshlrev_b64 v[32:33], 18, v[32:33]
	s_ashr_i32 s21, s20, 31
	s_ashr_i32 s23, s22, 31
	s_ashr_i32 s25, s24, 31
	s_lshl_b64 s[18:19], s[18:19], 10
	v_lshlrev_b64 v[34:35], 18, v[34:35]
	v_lshlrev_b64 v[50:51], 18, v[50:51]
	v_lshlrev_b64 v[52:53], 18, v[52:53]
	v_lshl_add_u64 v[32:33], s[4:5], 0, v[32:33]
	s_lshl_b64 s[20:21], s[20:21], 10
	s_lshl_b64 s[22:23], s[22:23], 10
	s_lshl_b64 s[24:25], s[24:25], 10
	v_lshl_add_u64 v[34:35], s[4:5], 0, v[34:35]
	v_lshl_add_u64 v[50:51], s[4:5], 0, v[50:51]
	v_lshl_add_u64 v[52:53], s[4:5], 0, v[52:53]
	v_lshl_add_u64 v[32:33], v[32:33], 0, s[18:19]
	v_lshl_add_u64 v[34:35], v[34:35], 0, s[20:21]
	v_lshl_add_u64 v[50:51], v[50:51], 0, s[22:23]
	v_lshl_add_u64 v[52:53], v[52:53], 0, s[24:25]
	v_lshl_add_u64 v[32:33], v[32:33], 0, v[18:19]
	v_lshl_add_u64 v[34:35], v[34:35], 0, v[18:19]
	v_lshl_add_u64 v[50:51], v[50:51], 0, v[18:19]
	v_lshl_add_u64 v[52:53], v[52:53], 0, v[18:19]
	global_load_dword v23, v[32:33], off nt
	global_load_dword v31, v[32:33], off offset:256 nt
	global_load_dword v56, v[32:33], off offset:512 nt
	global_load_dword v60, v[32:33], off offset:768 nt
	global_load_dword v64, v[34:35], off nt
	global_load_dword v68, v[34:35], off offset:256 nt
	global_load_dword v72, v[34:35], off offset:512 nt
	global_load_dword v76, v[34:35], off offset:768 nt
	global_load_dword v80, v[50:51], off nt
	global_load_dword v84, v[50:51], off offset:256 nt
	global_load_dword v88, v[50:51], off offset:512 nt
	global_load_dword v92, v[50:51], off offset:768 nt
	global_load_dword v96, v[52:53], off nt
	global_load_dword v100, v[52:53], off offset:256 nt
	global_load_dword v104, v[52:53], off offset:512 nt
	global_load_dword v108, v[52:53], off offset:768 nt
	s_waitcnt vmcnt(17)
	v_and_b32_e32 v141, 0xffff0000, v123
	v_lshlrev_b32_e32 v140, 16, v123
	v_and_b32_e32 v143, 0xffff0000, v128
	v_lshlrev_b32_e32 v142, 16, v128
	v_readfirstlane_b32 s38, v132
	v_readfirstlane_b32 s31, v135
	v_readfirstlane_b32 s28, v134
	v_readfirstlane_b32 s37, v133
	s_and_b32 s39, s38, 31
	s_and_b32 s41, s37, 31
	s_ashr_i32 s40, s28, 5
	s_and_b32 s28, s28, 31
	s_ashr_i32 s42, s31, 5
	s_and_b32 s31, s31, 31
	s_lshl_b32 s44, s39, 2
	s_lshl_b32 s45, s41, 2
	s_lshl_b32 s28, s28, 2
	s_lshl_b32 s31, s31, 2
	s_add_i32 s44, s1, s44
	s_add_i32 s45, s1, s45
	s_add_i32 s28, s1, s28
	s_add_i32 s31, s1, s31
	v_mov_b32_e32 v123, s44
	v_mov_b32_e32 v131, s45
	v_mov_b32_e32 v133, s28
	v_mov_b32_e32 v135, s31
	ds_read_b32 v132, v123
	ds_read_b32 v134, v131
	ds_read_b32 v150, v133
	ds_read_b32 v152, v135
	s_ashr_i32 s36, s38, 5
	s_waitcnt lgkmcnt(3)
	v_ashrrev_i32_e32 v133, 31, v132
	s_ashr_i32 s38, s37, 5
	s_ashr_i32 s37, s36, 31
	s_waitcnt lgkmcnt(2)
	v_ashrrev_i32_e32 v135, 31, v134
	s_waitcnt lgkmcnt(1)
	v_ashrrev_i32_e32 v151, 31, v150
	s_waitcnt lgkmcnt(0)
; #define GAS __attribute__((address_space(1)))
; __device__ __forceinline__ void p10_final(Frame& F, const Args& A) {
;     ...
;         for (int k = 0; k < 4; ++k) { const int e = pinfo4[k] & 31, pos = pinfo4[k] >> 5; const size_t row = (size_t)tpre[e] * 256 + pos; const float wk = pw4[k];
; #pragma unroll
;             for (int j = 0; j < 4; ++j) { const unsigned w = *(const GAS unsigned*)(Y + row * D + 256 * j + 4 * lane);
;                 const f32x2 a0 = __builtin_amdgcn_cvt_pk_f32_fp8((int)w, false), a1 = __builtin_amdgcn_cvt_pk_f32_fp8((int)w, true);
;                 v[4 * j] += wk * a0[0]; v[4 * j + 1] += wk * a0[1]; v[4 * j + 2] += wk * a1[0]; v[4 * j + 3] += wk * a1[1]; } }
;         float s = 0.f;
; #pragma unroll
;         for (int j = 0; j < 16; ++j) s += v[j] * v[j];
;         const float r = rsqrtf(wave_sum(s) * (1.0f / D) + EPS);
	v_ashrrev_i32_e32 v153, 31, v152
	v_lshlrev_b64 v[132:133], 18, v[132:133]
	s_ashr_i32 s39, s38, 31
	s_ashr_i32 s41, s40, 31
	s_ashr_i32 s43, s42, 31
	s_lshl_b64 s[36:37], s[36:37], 10
	v_lshlrev_b64 v[134:135], 18, v[134:135]
	v_lshlrev_b64 v[150:151], 18, v[150:151]
	v_lshlrev_b64 v[152:153], 18, v[152:153]
	v_lshl_add_u64 v[132:133], s[4:5], 0, v[132:133]
	s_lshl_b64 s[38:39], s[38:39], 10
	s_lshl_b64 s[40:41], s[40:41], 10
	s_lshl_b64 s[42:43], s[42:43], 10
	v_lshl_add_u64 v[134:135], s[4:5], 0, v[134:135]
	v_lshl_add_u64 v[150:151], s[4:5], 0, v[150:151]
	v_lshl_add_u64 v[152:153], s[4:5], 0, v[152:153]
	v_lshl_add_u64 v[132:133], v[132:133], 0, s[36:37]
	v_lshl_add_u64 v[134:135], v[134:135], 0, s[38:39]
	v_lshl_add_u64 v[150:151], v[150:151], 0, s[40:41]
	v_lshl_add_u64 v[152:153], v[152:153], 0, s[42:43]
	v_lshl_add_u64 v[132:133], v[132:133], 0, v[18:19]
	v_lshl_add_u64 v[134:135], v[134:135], 0, v[18:19]
	v_lshl_add_u64 v[150:151], v[150:151], 0, v[18:19]
	v_lshl_add_u64 v[152:153], v[152:153], 0, v[18:19]
	global_load_dword v123, v[132:133], off nt
	global_load_dword v131, v[132:133], off offset:256 nt
	global_load_dword v156, v[132:133], off offset:512 nt
	global_load_dword v160, v[132:133], off offset:768 nt
	global_load_dword v164, v[134:135], off nt
	global_load_dword v168, v[134:135], off offset:256 nt
	global_load_dword v172, v[134:135], off offset:512 nt
	global_load_dword v176, v[134:135], off offset:768 nt
	global_load_dword v180, v[150:151], off nt
	global_load_dword v184, v[150:151], off offset:256 nt
	global_load_dword v188, v[150:151], off offset:512 nt
	global_load_dword v192, v[150:151], off offset:768 nt
	global_load_dword v196, v[152:153], off nt
	global_load_dword v200, v[152:153], off offset:256 nt
	global_load_dword v204, v[152:153], off offset:512 nt
	global_load_dword v208, v[152:153], off offset:768 nt
	s_waitcnt vmcnt(16)
	v_and_b32_e32 v45, 0xffff0000, v29
	v_lshlrev_b32_e32 v44, 16, v29
	v_lshlrev_b32_e32 v28, 16, v26
	v_and_b32_e32 v29, 0xffff0000, v26
	v_lshlrev_b32_e32 v26, 16, v27
	v_and_b32_e32 v27, 0xffff0000, v27
	v_lshlrev_b32_e32 v46, 16, v24
	v_and_b32_e32 v47, 0xffff0000, v24
	v_lshlrev_b32_e32 v48, 16, v22
	v_and_b32_e32 v49, 0xffff0000, v22
	v_mov_b32_e32 v22, v39
	v_lshlrev_b32_e32 v24, 16, v25
	v_and_b32_e32 v25, 0xffff0000, v25
	v_cvt_pk_f32_fp8_e32 v[32:33], v23
	v_cvt_pk_f32_fp8_sdwa v[34:35], v23 src0_sel:WORD_1
	v_cvt_pk_f32_fp8_e32 v[50:51], v31
	v_cvt_pk_f32_fp8_sdwa v[52:53], v31 src0_sel:WORD_1
	v_cvt_pk_f32_fp8_e32 v[62:63], v64
	v_cvt_pk_f32_fp8_sdwa v[64:65], v64 src0_sel:WORD_1
	v_cvt_pk_f32_fp8_e32 v[66:67], v68
	v_pk_fma_f32 v[28:29], v[36:37], v[32:33], v[28:29] op_sel_hi:[0,1,1]
	v_cvt_pk_f32_fp8_e32 v[78:79], v80
	v_cvt_pk_f32_fp8_sdwa v[80:81], v80 src0_sel:WORD_1
	v_cvt_pk_f32_fp8_e32 v[54:55], v56
	v_cvt_pk_f32_fp8_e32 v[82:83], v84
	v_cvt_pk_f32_fp8_e32 v[94:95], v96
	v_cvt_pk_f32_fp8_sdwa v[96:97], v96 src0_sel:WORD_1
	v_pk_fma_f32 v[26:27], v[36:37], v[34:35], v[26:27] op_sel_hi:[0,1,1]
	v_pk_fma_f32 v[28:29], v[36:37], v[62:63], v[28:29] op_sel:[1,0,0]
	v_cvt_pk_f32_fp8_sdwa v[68:69], v68 src0_sel:WORD_1
	v_cvt_pk_f32_fp8_e32 v[98:99], v100
	v_pk_fma_f32 v[26:27], v[36:37], v[64:65], v[26:27] op_sel:[1,0,0]
	v_pk_fma_f32 v[28:29], v[38:39], v[78:79], v[28:29] op_sel_hi:[0,1,1]
	v_cvt_pk_f32_fp8_sdwa v[56:57], v56 src0_sel:WORD_1
	v_cvt_pk_f32_fp8_e32 v[58:59], v60
	v_cvt_pk_f32_fp8_sdwa v[60:61], v60 src0_sel:WORD_1
	v_cvt_pk_f32_fp8_sdwa v[84:85], v84 src0_sel:WORD_1
	v_pk_fma_f32 v[32:33], v[36:37], v[50:51], v[46:47] op_sel_hi:[0,1,1]
	v_pk_fma_f32 v[26:27], v[38:39], v[80:81], v[26:27] op_sel_hi:[0,1,1]
	v_pk_fma_f32 v[28:29], v[22:23], v[94:95], v[28:29] op_sel_hi:[0,1,1]
	v_cvt_pk_f32_fp8_e32 v[70:71], v72
	v_cvt_pk_f32_fp8_sdwa v[72:73], v72 src0_sel:WORD_1
	v_cvt_pk_f32_fp8_e32 v[74:75], v76
	v_cvt_pk_f32_fp8_sdwa v[76:77], v76 src0_sel:WORD_1
	v_cvt_pk_f32_fp8_sdwa v[100:101], v100 src0_sel:WORD_1
	v_pk_fma_f32 v[32:33], v[36:37], v[66:67], v[32:33] op_sel:[1,0,0]
	v_pk_fma_f32 v[26:27], v[22:23], v[96:97], v[26:27] op_sel_hi:[0,1,1]
	v_pk_mul_f32 v[46:47], v[28:29], v[28:29]
	v_cvt_pk_f32_fp8_e32 v[86:87], v88
	v_cvt_pk_f32_fp8_sdwa v[88:89], v88 src0_sel:WORD_1
	v_cvt_pk_f32_fp8_e32 v[90:91], v92
	v_cvt_pk_f32_fp8_sdwa v[92:93], v92 src0_sel:WORD_1
	v_pk_fma_f32 v[24:25], v[36:37], v[52:53], v[24:25] op_sel_hi:[0,1,1]
	v_pk_fma_f32 v[34:35], v[36:37], v[54:55], v[48:49] op_sel_hi:[0,1,1]
	v_pk_fma_f32 v[32:33], v[38:39], v[82:83], v[32:33] op_sel_hi:[0,1,1]
	v_pk_mul_f32 v[48:49], v[26:27], v[26:27]
	v_add_f32_e32 v31, v46, v47
	v_cvt_pk_f32_fp8_e32 v[102:103], v104
	v_cvt_pk_f32_fp8_sdwa v[104:105], v104 src0_sel:WORD_1
	v_cvt_pk_f32_fp8_e32 v[106:107], v108
	v_cvt_pk_f32_fp8_sdwa v[108:109], v108 src0_sel:WORD_1
	v_pk_fma_f32 v[24:25], v[36:37], v[68:69], v[24:25] op_sel:[1,0,0]
	v_pk_fma_f32 v[32:33], v[22:23], v[98:99], v[32:33] op_sel_hi:[0,1,1]
	v_add_f32_e32 v31, v31, v48
	v_pk_fma_f32 v[40:41], v[36:37], v[56:57], v[40:41] op_sel_hi:[0,1,1]
	v_pk_fma_f32 v[42:43], v[36:37], v[58:59], v[42:43] op_sel_hi:[0,1,1]
	v_pk_fma_f32 v[44:45], v[36:37], v[60:61], v[44:45] op_sel_hi:[0,1,1]
	v_pk_fma_f32 v[24:25], v[38:39], v[84:85], v[24:25] op_sel_hi:[0,1,1]
	v_pk_mul_f32 v[50:51], v[32:33], v[32:33]
	v_add_f32_e32 v31, v49, v31
	v_pk_fma_f32 v[40:41], v[36:37], v[72:73], v[40:41] op_sel:[1,0,0]
	v_pk_fma_f32 v[42:43], v[36:37], v[74:75], v[42:43] op_sel:[1,0,0]
	v_pk_fma_f32 v[44:45], v[36:37], v[76:77], v[44:45] op_sel:[1,0,0]
	v_pk_fma_f32 v[34:35], v[36:37], v[70:71], v[34:35] op_sel:[1,0,0]
	v_pk_fma_f32 v[24:25], v[22:23], v[100:101], v[24:25] op_sel_hi:[0,1,1]
; #define GAS __attribute__((address_space(1)))
; __device__ __forceinline__ void p10_final(Frame& F, const Args& A) {
;     ...
;     for (int t = gw; t < T; t += NGW) {
;         float v[16];
;         const int4 pi = *(const int4*)(pinf + 4 * t); const f32x4 pw4 = *(const f32x4*)(pwt + 4 * t);
;         const int pinfo4[4] = {pi.x, pi.y, pi.z, pi.w};
; #pragma unroll
;         for (int j = 0; j < 4; ++j) { const u32x2 w = *(const GAS u32x2*)(x2b + (size_t)t * D + 256 * j + 4 * lane);
;             v[4 * j] = bflo(w.x); v[4 * j + 1] = bfhi(w.x); v[4 * j + 2] = bflo(w.y); v[4 * j + 3] = bfhi(w.y); }
; #pragma unroll
;         for (int k = 0; k < 4; ++k) { const int e = pinfo4[k] & 31, pos = pinfo4[k] >> 5; const size_t row = (size_t)tpre[e] * 256 + pos; const float wk = pw4[k];
; #pragma unroll
;             for (int j = 0; j < 4; ++j) { const unsigned w = *(const GAS unsigned*)(Y + row * D + 256 * j + 4 * lane);
;                 const f32x2 a0 = __builtin_amdgcn_cvt_pk_f32_fp8((int)w, false), a1 = __builtin_amdgcn_cvt_pk_f32_fp8((int)w, true);
;                 v[4 * j] += wk * a0[0]; v[4 * j + 1] += wk * a0[1]; v[4 * j + 2] += wk * a1[0]; v[4 * j + 3] += wk * a1[1]; } }
;         float s = 0.f;
; #pragma unroll
;         for (int j = 0; j < 16; ++j) s += v[j] * v[j];
;         const float r = rsqrtf(wave_sum(s) * (1.0f / D) + EPS);
; #pragma unroll
;         for (int j = 0; j < 4; ++j)
;             __builtin_nontemporal_store((f32x4){v[4 * j] * r * g[j][0], v[4 * j + 1] * r * g[j][1], v[4 * j + 2] * r * g[j][2], v[4 * j + 3] * r * g[j][3]}, (GAS f32x4*)(out + (size_t)t * D + 256 * j + 4 * lane));
	v_add_f32_e32 v31, v31, v50
	v_pk_fma_f32 v[36:37], v[38:39], v[88:89], v[40:41] op_sel_hi:[0,1,1]
	v_pk_fma_f32 v[40:41], v[38:39], v[90:91], v[42:43] op_sel_hi:[0,1,1]
	v_pk_fma_f32 v[42:43], v[38:39], v[92:93], v[44:45] op_sel_hi:[0,1,1]
	v_pk_fma_f32 v[34:35], v[38:39], v[86:87], v[34:35] op_sel_hi:[0,1,1]
	v_pk_mul_f32 v[52:53], v[24:25], v[24:25]
	v_add_f32_e32 v31, v51, v31
	v_pk_fma_f32 v[36:37], v[22:23], v[104:105], v[36:37] op_sel_hi:[0,1,1]
	v_pk_fma_f32 v[38:39], v[22:23], v[106:107], v[40:41] op_sel_hi:[0,1,1]
	v_pk_fma_f32 v[40:41], v[22:23], v[108:109], v[42:43] op_sel_hi:[0,1,1]
	v_pk_fma_f32 v[22:23], v[22:23], v[102:103], v[34:35] op_sel_hi:[0,1,1]
	v_add_f32_e32 v31, v52, v31
	v_pk_mul_f32 v[54:55], v[22:23], v[22:23]
	v_add_f32_e32 v31, v53, v31
	v_add_f32_e32 v31, v54, v31
	v_pk_mul_f32 v[34:35], v[36:37], v[36:37]
	v_add_f32_e32 v31, v55, v31
	v_add_f32_e32 v31, v34, v31
	v_pk_mul_f32 v[42:43], v[38:39], v[38:39]
	v_add_f32_e32 v31, v35, v31
	v_add_f32_e32 v31, v42, v31
	v_pk_mul_f32 v[44:45], v[40:41], v[40:41]
	v_add_f32_e32 v31, v43, v31
	v_add_f32_e32 v31, v44, v31
	v_add_f32_e32 v31, v45, v31
	s_nop 1
	v_add_f32_dpp v31, v31, v31 row_ror:1 row_mask:0xf bank_mask:0xf bound_ctrl:1
	s_nop 1
	v_add_f32_dpp v31, v31, v31 row_ror:2 row_mask:0xf bank_mask:0xf bound_ctrl:1
	s_nop 1
	v_add_f32_dpp v31, v31, v31 row_ror:4 row_mask:0xf bank_mask:0xf bound_ctrl:1
	s_nop 1
	v_add_f32_dpp v31, v31, v31 row_ror:8 row_mask:0xf bank_mask:0xf bound_ctrl:1
	s_nop 0
	v_readlane_b32 s7, v31, 16
	v_readlane_b32 s17, v31, 48
	v_readlane_b32 s18, v31, 0
	v_readlane_b32 s19, v31, 32
	v_mov_b32_e32 v34, s7
	v_mov_b32_e32 v35, s17
	v_pk_add_f32 v[34:35], s[18:19], v[34:35]
	s_nop 0
	v_add_f32_e32 v31, v34, v35
	v_fmamk_f32 v31, v31, 0x3a800000, v30
	v_mul_f32_e32 v34, 0x4b800000, v31
	v_cmp_gt_f32_e32 vcc, s3, v31
	s_nop 1
	v_cndmask_b32_e32 v31, v31, v34, vcc
	v_rsq_f32_e32 v31, v31
	s_nop 0
	v_mul_f32_e32 v34, 0x45800000, v31
	v_cndmask_b32_e32 v34, v31, v34, vcc
	v_pk_mul_f32 v[28:29], v[28:29], v[34:35] op_sel_hi:[1,0]
	v_pk_mul_f32 v[26:27], v[26:27], v[34:35] op_sel_hi:[1,0]
	v_pk_mul_f32 v[32:33], v[32:33], v[34:35] op_sel_hi:[1,0]
	v_pk_mul_f32 v[42:43], v[24:25], v[34:35] op_sel_hi:[1,0]
	v_pk_mul_f32 v[44:45], v[22:23], v[34:35] op_sel_hi:[1,0]
	v_pk_mul_f32 v[36:37], v[36:37], v[34:35] op_sel_hi:[1,0]
	v_pk_mul_f32 v[46:47], v[38:39], v[34:35] op_sel_hi:[1,0]
	v_pk_mul_f32 v[38:39], v[40:41], v[34:35] op_sel_hi:[1,0]
	v_pk_mul_f32 v[24:25], v[16:17], v[26:27]
	v_pk_mul_f32 v[22:23], v[14:15], v[28:29]
	v_pk_mul_f32 v[28:29], v[12:13], v[42:43]
	v_pk_mul_f32 v[26:27], v[10:11], v[32:33]
	v_pk_mul_f32 v[34:35], v[8:9], v[36:37]
	v_pk_mul_f32 v[32:33], v[6:7], v[44:45]
	v_pk_mul_f32 v[38:39], v[4:5], v[38:39]
	v_pk_mul_f32 v[36:37], v[2:3], v[46:47]
	global_store_dwordx4 v[0:1], v[22:25], off offset:-3072 nt
	global_store_dwordx4 v[0:1], v[26:29], off offset:-2048 nt
	global_store_dwordx4 v[0:1], v[32:35], off offset:-1024 nt
	global_store_dwordx4 v[0:1], v[36:39], off nt
	s_waitcnt vmcnt(4)
	v_and_b32_e32 v145, 0xffff0000, v129
	v_lshlrev_b32_e32 v144, 16, v129
	v_lshlrev_b32_e32 v128, 16, v126
	v_and_b32_e32 v129, 0xffff0000, v126
	v_lshlrev_b32_e32 v126, 16, v127
	v_and_b32_e32 v127, 0xffff0000, v127
	v_lshlrev_b32_e32 v146, 16, v124
	v_and_b32_e32 v147, 0xffff0000, v124
	v_lshlrev_b32_e32 v148, 16, v122
	v_and_b32_e32 v149, 0xffff0000, v122
	v_mov_b32_e32 v122, v139
	v_lshlrev_b32_e32 v124, 16, v125
	v_and_b32_e32 v125, 0xffff0000, v125
	v_cvt_pk_f32_fp8_e32 v[132:133], v123
	v_cvt_pk_f32_fp8_sdwa v[134:135], v123 src0_sel:WORD_1
	v_cvt_pk_f32_fp8_e32 v[150:151], v131
	v_cvt_pk_f32_fp8_sdwa v[152:153], v131 src0_sel:WORD_1
	v_cvt_pk_f32_fp8_e32 v[162:163], v164
	v_cvt_pk_f32_fp8_sdwa v[164:165], v164 src0_sel:WORD_1
	v_cvt_pk_f32_fp8_e32 v[166:167], v168
	v_pk_fma_f32 v[128:129], v[136:137], v[132:133], v[128:129] op_sel_hi:[0,1,1]
	v_cvt_pk_f32_fp8_e32 v[178:179], v180
	v_cvt_pk_f32_fp8_sdwa v[180:181], v180 src0_sel:WORD_1
	v_cvt_pk_f32_fp8_e32 v[154:155], v156
	v_cvt_pk_f32_fp8_e32 v[182:183], v184
	v_cvt_pk_f32_fp8_e32 v[194:195], v196
	v_cvt_pk_f32_fp8_sdwa v[196:197], v196 src0_sel:WORD_1
	v_pk_fma_f32 v[126:127], v[136:137], v[134:135], v[126:127] op_sel_hi:[0,1,1]
	v_pk_fma_f32 v[128:129], v[136:137], v[162:163], v[128:129] op_sel:[1,0,0]
	v_cvt_pk_f32_fp8_sdwa v[168:169], v168 src0_sel:WORD_1
	v_cvt_pk_f32_fp8_e32 v[198:199], v200
	v_pk_fma_f32 v[126:127], v[136:137], v[164:165], v[126:127] op_sel:[1,0,0]
	v_pk_fma_f32 v[128:129], v[138:139], v[178:179], v[128:129] op_sel_hi:[0,1,1]
	v_cvt_pk_f32_fp8_sdwa v[156:157], v156 src0_sel:WORD_1
	v_cvt_pk_f32_fp8_e32 v[158:159], v160
	v_cvt_pk_f32_fp8_sdwa v[160:161], v160 src0_sel:WORD_1
	v_cvt_pk_f32_fp8_sdwa v[184:185], v184 src0_sel:WORD_1
	v_pk_fma_f32 v[132:133], v[136:137], v[150:151], v[146:147] op_sel_hi:[0,1,1]
	v_pk_fma_f32 v[126:127], v[138:139], v[180:181], v[126:127] op_sel_hi:[0,1,1]
	v_pk_fma_f32 v[128:129], v[122:123], v[194:195], v[128:129] op_sel_hi:[0,1,1]
	v_cvt_pk_f32_fp8_e32 v[170:171], v172
	v_cvt_pk_f32_fp8_sdwa v[172:173], v172 src0_sel:WORD_1
	v_cvt_pk_f32_fp8_e32 v[174:175], v176
	v_cvt_pk_f32_fp8_sdwa v[176:177], v176 src0_sel:WORD_1
	v_cvt_pk_f32_fp8_sdwa v[200:201], v200 src0_sel:WORD_1
; #define GAS __attribute__((address_space(1)))
; __device__ __forceinline__ void p10_final(Frame& F, const Args& A) {
;     ...
;     for (int t = gw; t < T; t += NGW) {
;         float v[16];
;         const int4 pi = *(const int4*)(pinf + 4 * t); const f32x4 pw4 = *(const f32x4*)(pwt + 4 * t);
;         const int pinfo4[4] = {pi.x, pi.y, pi.z, pi.w};
; #pragma unroll
;         for (int j = 0; j < 4; ++j) { const u32x2 w = *(const GAS u32x2*)(x2b + (size_t)t * D + 256 * j + 4 * lane);
;             v[4 * j] = bflo(w.x); v[4 * j + 1] = bfhi(w.x); v[4 * j + 2] = bflo(w.y); v[4 * j + 3] = bfhi(w.y); }
; #pragma unroll
;         for (int k = 0; k < 4; ++k) { const int e = pinfo4[k] & 31, pos = pinfo4[k] >> 5; const size_t row = (size_t)tpre[e] * 256 + pos; const float wk = pw4[k];
; #pragma unroll
;             for (int j = 0; j < 4; ++j) { const unsigned w = *(const GAS unsigned*)(Y + row * D + 256 * j + 4 * lane);
;                 const f32x2 a0 = __builtin_amdgcn_cvt_pk_f32_fp8((int)w, false), a1 = __builtin_amdgcn_cvt_pk_f32_fp8((int)w, true);
;                 v[4 * j] += wk * a0[0]; v[4 * j + 1] += wk * a0[1]; v[4 * j + 2] += wk * a1[0]; v[4 * j + 3] += wk * a1[1]; } }
;         float s = 0.f;
; #pragma unroll
;         for (int j = 0; j < 16; ++j) s += v[j] * v[j];
;         const float r = rsqrtf(wave_sum(s) * (1.0f / D) + EPS);
; #pragma unroll
;         for (int j = 0; j < 4; ++j)
;             __builtin_nontemporal_store((f32x4){v[4 * j] * r * g[j][0], v[4 * j + 1] * r * g[j][1], v[4 * j + 2] * r * g[j][2], v[4 * j + 3] * r * g[j][3]}, (GAS f32x4*)(out + (size_t)t * D + 256 * j + 4 * lane));
	v_pk_fma_f32 v[132:133], v[136:137], v[166:167], v[132:133] op_sel:[1,0,0]
	v_pk_fma_f32 v[126:127], v[122:123], v[196:197], v[126:127] op_sel_hi:[0,1,1]
	v_pk_mul_f32 v[146:147], v[128:129], v[128:129]
	v_cvt_pk_f32_fp8_e32 v[186:187], v188
	v_cvt_pk_f32_fp8_sdwa v[188:189], v188 src0_sel:WORD_1
	v_cvt_pk_f32_fp8_e32 v[190:191], v192
	v_cvt_pk_f32_fp8_sdwa v[192:193], v192 src0_sel:WORD_1
	v_pk_fma_f32 v[124:125], v[136:137], v[152:153], v[124:125] op_sel_hi:[0,1,1]
	v_pk_fma_f32 v[134:135], v[136:137], v[154:155], v[148:149] op_sel_hi:[0,1,1]
	v_pk_fma_f32 v[132:133], v[138:139], v[182:183], v[132:133] op_sel_hi:[0,1,1]
	v_pk_mul_f32 v[148:149], v[126:127], v[126:127]
	v_add_f32_e32 v131, v146, v147
	v_cvt_pk_f32_fp8_e32 v[202:203], v204
	v_cvt_pk_f32_fp8_sdwa v[204:205], v204 src0_sel:WORD_1
	v_cvt_pk_f32_fp8_e32 v[206:207], v208
	v_cvt_pk_f32_fp8_sdwa v[208:209], v208 src0_sel:WORD_1
	v_pk_fma_f32 v[124:125], v[136:137], v[168:169], v[124:125] op_sel:[1,0,0]
	v_pk_fma_f32 v[132:133], v[122:123], v[198:199], v[132:133] op_sel_hi:[0,1,1]
	v_add_f32_e32 v131, v131, v148
	v_pk_fma_f32 v[140:141], v[136:137], v[156:157], v[140:141] op_sel_hi:[0,1,1]
	v_pk_fma_f32 v[142:143], v[136:137], v[158:159], v[142:143] op_sel_hi:[0,1,1]
	v_pk_fma_f32 v[144:145], v[136:137], v[160:161], v[144:145] op_sel_hi:[0,1,1]
	v_pk_fma_f32 v[124:125], v[138:139], v[184:185], v[124:125] op_sel_hi:[0,1,1]
	v_pk_mul_f32 v[150:151], v[132:133], v[132:133]
	v_add_f32_e32 v131, v149, v131
	v_pk_fma_f32 v[140:141], v[136:137], v[172:173], v[140:141] op_sel:[1,0,0]
	v_pk_fma_f32 v[142:143], v[136:137], v[174:175], v[142:143] op_sel:[1,0,0]
	v_pk_fma_f32 v[144:145], v[136:137], v[176:177], v[144:145] op_sel:[1,0,0]
	v_pk_fma_f32 v[134:135], v[136:137], v[170:171], v[134:135] op_sel:[1,0,0]
	v_pk_fma_f32 v[124:125], v[122:123], v[200:201], v[124:125] op_sel_hi:[0,1,1]
	v_add_f32_e32 v131, v131, v150
	v_pk_fma_f32 v[136:137], v[138:139], v[188:189], v[140:141] op_sel_hi:[0,1,1]
	v_pk_fma_f32 v[140:141], v[138:139], v[190:191], v[142:143] op_sel_hi:[0,1,1]
	v_pk_fma_f32 v[142:143], v[138:139], v[192:193], v[144:145] op_sel_hi:[0,1,1]
	v_pk_fma_f32 v[134:135], v[138:139], v[186:187], v[134:135] op_sel_hi:[0,1,1]
	v_pk_mul_f32 v[152:153], v[124:125], v[124:125]
	v_add_f32_e32 v131, v151, v131
	v_pk_fma_f32 v[136:137], v[122:123], v[204:205], v[136:137] op_sel_hi:[0,1,1]
	v_pk_fma_f32 v[138:139], v[122:123], v[206:207], v[140:141] op_sel_hi:[0,1,1]
	v_pk_fma_f32 v[140:141], v[122:123], v[208:209], v[142:143] op_sel_hi:[0,1,1]
	v_pk_fma_f32 v[122:123], v[122:123], v[202:203], v[134:135] op_sel_hi:[0,1,1]
	v_add_f32_e32 v131, v152, v131
	v_pk_mul_f32 v[154:155], v[122:123], v[122:123]
	v_add_f32_e32 v131, v153, v131
	v_add_f32_e32 v131, v154, v131
	v_pk_mul_f32 v[134:135], v[136:137], v[136:137]
	v_add_f32_e32 v131, v155, v131
	v_add_f32_e32 v131, v134, v131
	v_pk_mul_f32 v[142:143], v[138:139], v[138:139]
	v_add_f32_e32 v131, v135, v131
	v_add_f32_e32 v131, v142, v131
	v_pk_mul_f32 v[144:145], v[140:141], v[140:141]
	v_add_f32_e32 v131, v143, v131
	v_add_f32_e32 v131, v144, v131
	v_add_f32_e32 v131, v145, v131
	s_nop 1
	v_add_f32_dpp v131, v131, v131 row_ror:1 row_mask:0xf bank_mask:0xf bound_ctrl:1
	s_nop 1
	v_add_f32_dpp v131, v131, v131 row_ror:2 row_mask:0xf bank_mask:0xf bound_ctrl:1
	s_nop 1
	v_add_f32_dpp v131, v131, v131 row_ror:4 row_mask:0xf bank_mask:0xf bound_ctrl:1
	s_nop 1
	v_add_f32_dpp v131, v131, v131 row_ror:8 row_mask:0xf bank_mask:0xf bound_ctrl:1
	s_nop 0
	v_readlane_b32 s31, v131, 16
	v_readlane_b32 s28, v131, 48
	v_readlane_b32 s36, v131, 0
	v_readlane_b32 s37, v131, 32
	v_mov_b32_e32 v134, s31
	v_mov_b32_e32 v135, s28
	v_pk_add_f32 v[134:135], s[36:37], v[134:135]
	s_nop 0
	v_add_f32_e32 v131, v134, v135
	v_fmamk_f32 v131, v131, 0x3a800000, v30
	v_mul_f32_e32 v134, 0x4b800000, v131
	v_cmp_gt_f32_e32 vcc, s3, v131
	s_nop 1
	v_cndmask_b32_e32 v131, v131, v134, vcc
	v_rsq_f32_e32 v131, v131
	s_nop 0
	v_mul_f32_e32 v134, 0x45800000, v131
	v_cndmask_b32_e32 v134, v131, v134, vcc
	v_pk_mul_f32 v[128:129], v[128:129], v[134:135] op_sel_hi:[1,0]
	v_pk_mul_f32 v[126:127], v[126:127], v[134:135] op_sel_hi:[1,0]
	v_pk_mul_f32 v[132:133], v[132:133], v[134:135] op_sel_hi:[1,0]
	v_pk_mul_f32 v[142:143], v[124:125], v[134:135] op_sel_hi:[1,0]
	v_pk_mul_f32 v[144:145], v[122:123], v[134:135] op_sel_hi:[1,0]
	v_pk_mul_f32 v[136:137], v[136:137], v[134:135] op_sel_hi:[1,0]
	v_pk_mul_f32 v[146:147], v[138:139], v[134:135] op_sel_hi:[1,0]
	v_pk_mul_f32 v[138:139], v[140:141], v[134:135] op_sel_hi:[1,0]
	v_pk_mul_f32 v[124:125], v[16:17], v[126:127]
	v_pk_mul_f32 v[122:123], v[14:15], v[128:129]
	v_pk_mul_f32 v[128:129], v[12:13], v[142:143]
	v_pk_mul_f32 v[126:127], v[10:11], v[132:133]
	v_pk_mul_f32 v[134:135], v[8:9], v[136:137]
	v_pk_mul_f32 v[132:133], v[6:7], v[144:145]
	v_pk_mul_f32 v[138:139], v[4:5], v[138:139]
	v_pk_mul_f32 v[136:137], v[2:3], v[146:147]
	global_store_dwordx4 v[118:119], v[122:125], off offset:-3072 nt
	global_store_dwordx4 v[118:119], v[126:129], off offset:-2048 nt
	global_store_dwordx4 v[118:119], v[132:135], off offset:-1024 nt
	global_store_dwordx4 v[118:119], v[136:139], off nt
	v_lshl_add_u64 v[0:1], v[118:119], 0, s[8:9]
	s_cmp_lt_i32 s0, 0x10000
	s_cbranch_scc1 .LBB0_1146
